# final rowpass: nontemporal stores for the f32 output (written once, never re-read by the kernel)
# speedup vs baseline: 1.0038x; 1.0038x over previous
.LBB0_3809:
	v_cvt_pk_f32_fp8_sdwa v[134:135], v111 src0_sel:WORD_1
	v_cvt_pk_f32_fp8_sdwa v[148:149], v113 src0_sel:WORD_1
	v_cvt_pk_f32_fp8_sdwa v[162:163], v118 src0_sel:WORD_1
	v_cvt_pk_f32_fp8_e32 v[172:173], v122
	v_cvt_pk_f32_fp8_sdwa v[122:123], v122 src0_sel:WORD_1
	v_cvt_f32_f16_sdwa v125, v81 dst_sel:DWORD dst_unused:UNUSED_PAD src0_sel:WORD_1
	v_cvt_f32_f16_sdwa v127, v80 dst_sel:DWORD dst_unused:UNUSED_PAD src0_sel:WORD_1
	v_cvt_f32_f16_e32 v124, v81
	v_cvt_f32_f16_e32 v126, v80
	v_cvt_f32_f16_sdwa v81, v79 dst_sel:DWORD dst_unused:UNUSED_PAD src0_sel:WORD_1
	v_cvt_f32_f16_sdwa v129, v78 dst_sel:DWORD dst_unused:UNUSED_PAD src0_sel:WORD_1
	v_cvt_f32_f16_e32 v80, v79
	v_cvt_f32_f16_e32 v128, v78
	v_cvt_f32_f16_sdwa v79, v77 dst_sel:DWORD dst_unused:UNUSED_PAD src0_sel:WORD_1
	v_cvt_f32_f16_sdwa v131, v76 dst_sel:DWORD dst_unused:UNUSED_PAD src0_sel:WORD_1
	v_cvt_f32_f16_e32 v78, v77
	v_cvt_f32_f16_e32 v130, v76
	v_cvt_f32_f16_sdwa v77, v75 dst_sel:DWORD dst_unused:UNUSED_PAD src0_sel:WORD_1
	v_cvt_f32_f16_sdwa v133, v74 dst_sel:DWORD dst_unused:UNUSED_PAD src0_sel:WORD_1
	v_cvt_f32_f16_e32 v76, v75
	v_cvt_f32_f16_e32 v132, v74
	v_cvt_pk_f32_fp8_e32 v[74:75], v111
	v_cvt_pk_f32_fp8_e32 v[136:137], v110
	v_cvt_pk_f32_fp8_sdwa v[110:111], v110 src0_sel:WORD_1
	v_pk_fma_f32 v[134:135], v[70:71], v[134:135], 0 op_sel:[1,0,0] op_sel_hi:[1,1,0]
	v_cvt_pk_f32_fp8_sdwa v[152:153], v114 src0_sel:WORD_1
	v_pk_fma_f32 v[134:135], v[70:71], v[148:149], v[134:135] op_sel_hi:[0,1,1]
	v_cvt_pk_f32_fp8_e32 v[150:151], v114
	v_cvt_pk_f32_fp8_e32 v[160:161], v118
	v_cvt_pk_f32_fp8_e32 v[164:165], v119
	v_cvt_pk_f32_fp8_sdwa v[118:119], v119 src0_sel:WORD_1
	v_pk_fma_f32 v[134:135], v[72:73], v[162:163], v[134:135] op_sel:[1,0,0]
	v_cvt_pk_f32_fp8_sdwa v[140:141], v109 src0_sel:WORD_1
	v_pk_fma_f32 v[122:123], v[72:73], v[122:123], v[134:135] op_sel_hi:[0,1,1]
	v_cvt_pk_f32_fp8_e32 v[134:135], v115
	v_cvt_pk_f32_fp8_sdwa v[114:115], v115 src0_sel:WORD_1
	v_pk_fma_f32 v[110:111], v[70:71], v[110:111], 0 op_sel:[1,0,0] op_sel_hi:[1,1,0]
	v_cvt_pk_f32_fp8_e32 v[138:139], v109
	v_cvt_pk_f32_fp8_sdwa v[156:157], v116 src0_sel:WORD_1
	v_pk_fma_f32 v[136:137], v[70:71], v[136:137], 0 op_sel:[1,0,0] op_sel_hi:[1,1,0]
	v_pk_fma_f32 v[110:111], v[70:71], v[152:153], v[110:111] op_sel_hi:[0,1,1]
	v_cvt_pk_f32_fp8_e32 v[154:155], v116
	v_cvt_pk_f32_fp8_sdwa v[168:169], v120 src0_sel:WORD_1
	v_pk_fma_f32 v[136:137], v[70:71], v[150:151], v[136:137] op_sel_hi:[0,1,1]
	v_pk_fma_f32 v[110:111], v[72:73], v[118:119], v[110:111] op_sel:[1,0,0]
	v_cvt_pk_f32_fp8_e32 v[146:147], v113
	v_cvt_pk_f32_fp8_e32 v[166:167], v120
	v_pk_fma_f32 v[118:119], v[72:73], v[164:165], v[136:137] op_sel:[1,0,0]
	v_pk_fma_f32 v[110:111], v[72:73], v[114:115], v[110:111] op_sel_hi:[0,1,1]
	v_cvt_pk_f32_fp8_e32 v[114:115], v112
	v_cvt_pk_f32_fp8_sdwa v[112:113], v112 src0_sel:WORD_1
	v_cvt_pk_f32_fp8_e32 v[142:143], v107
	v_cvt_pk_f32_fp8_sdwa v[144:145], v107 src0_sel:WORD_1
	v_pk_fma_f32 v[118:119], v[72:73], v[134:135], v[118:119] op_sel_hi:[0,1,1]
	v_pk_fma_f32 v[134:135], v[70:71], v[140:141], 0 op_sel:[1,0,0] op_sel_hi:[1,1,0]
	v_cvt_pk_f32_fp8_e32 v[158:159], v117
	v_cvt_pk_f32_fp8_sdwa v[116:117], v117 src0_sel:WORD_1
	v_pk_fma_f32 v[136:137], v[70:71], v[138:139], 0 op_sel:[1,0,0] op_sel_hi:[1,1,0]
	v_pk_fma_f32 v[134:135], v[70:71], v[156:157], v[134:135] op_sel_hi:[0,1,1]
	v_cvt_pk_f32_fp8_e32 v[170:171], v121
	v_cvt_pk_f32_fp8_sdwa v[120:121], v121 src0_sel:WORD_1
	v_pk_fma_f32 v[136:137], v[70:71], v[154:155], v[136:137] op_sel_hi:[0,1,1]
	v_pk_fma_f32 v[134:135], v[72:73], v[168:169], v[134:135] op_sel:[1,0,0]
	v_pk_fma_f32 v[74:75], v[70:71], v[74:75], 0 op_sel:[1,0,0] op_sel_hi:[1,1,0]
	v_pk_fma_f32 v[136:137], v[72:73], v[166:167], v[136:137] op_sel:[1,0,0]
	v_pk_fma_f32 v[112:113], v[72:73], v[112:113], v[134:135] op_sel_hi:[0,1,1]
	v_cvt_pk_f32_fp8_e32 v[134:135], v108
	v_cvt_pk_f32_fp8_sdwa v[108:109], v108 src0_sel:WORD_1
	v_pk_fma_f32 v[74:75], v[70:71], v[146:147], v[74:75] op_sel_hi:[0,1,1]
	v_pk_fma_f32 v[114:115], v[72:73], v[114:115], v[136:137] op_sel_hi:[0,1,1]
	v_pk_fma_f32 v[136:137], v[70:71], v[144:145], 0 op_sel:[1,0,0] op_sel_hi:[1,1,0]
	v_pk_fma_f32 v[138:139], v[70:71], v[142:143], 0 op_sel:[1,0,0] op_sel_hi:[1,1,0]
	v_pk_fma_f32 v[74:75], v[72:73], v[160:161], v[74:75] op_sel:[1,0,0]
	v_pk_fma_f32 v[138:139], v[70:71], v[158:159], v[138:139] op_sel_hi:[0,1,1]
	v_pk_fma_f32 v[70:71], v[70:71], v[116:117], v[136:137] op_sel_hi:[0,1,1]
	v_pk_fma_f32 v[74:75], v[72:73], v[172:173], v[74:75] op_sel_hi:[0,1,1]
	v_pk_fma_f32 v[70:71], v[72:73], v[120:121], v[70:71] op_sel:[1,0,0]
	v_pk_fma_f32 v[116:117], v[72:73], v[170:171], v[138:139] op_sel:[1,0,0]
	v_pk_fma_f32 v[70:71], v[72:73], v[108:109], v[70:71] op_sel_hi:[0,1,1]
	v_pk_fma_f32 v[116:117], v[72:73], v[134:135], v[116:117] op_sel_hi:[0,1,1]
	v_pk_mul_f32 v[72:73], v[2:3], v[122:123]
	v_pk_mul_f32 v[74:75], v[0:1], v[74:75]
	v_pk_fma_f32 v[72:73], v[124:125], s[26:27], v[72:73] op_sel_hi:[1,0,1]
	v_pk_fma_f32 v[74:75], v[126:127], s[26:27], v[74:75] op_sel_hi:[1,0,1]
	v_add_f32_e32 v108, v72, v73
	v_add_f32_e32 v107, v74, v75
	v_add_f32_e32 v107, v107, v108
	v_pk_mul_f32 v[108:109], v[6:7], v[110:111]
	v_pk_mul_f32 v[110:111], v[4:5], v[118:119]
	v_pk_fma_f32 v[80:81], v[80:81], s[26:27], v[108:109] op_sel_hi:[1,0,1]
	v_pk_fma_f32 v[110:111], v[128:129], s[26:27], v[110:111] op_sel_hi:[1,0,1]
	v_add_f32_e32 v109, v80, v81
	v_add_f32_e32 v108, v110, v111
	v_add_f32_e32 v107, 0, v107
	v_add_f32_e32 v108, v108, v109
	v_add_f32_e32 v107, v107, v108
	v_pk_mul_f32 v[108:109], v[10:11], v[112:113]
	v_pk_mul_f32 v[112:113], v[8:9], v[114:115]
	v_pk_fma_f32 v[78:79], v[78:79], s[26:27], v[108:109] op_sel_hi:[1,0,1]
	v_pk_fma_f32 v[112:113], v[130:131], s[26:27], v[112:113] op_sel_hi:[1,0,1]
	v_add_f32_e32 v109, v78, v79
	v_add_f32_e32 v108, v112, v113
	v_add_f32_e32 v108, v108, v109
	v_add_f32_e32 v107, v107, v108
	v_pk_mul_f32 v[70:71], v[14:15], v[70:71]
	v_pk_mul_f32 v[108:109], v[12:13], v[116:117]
	v_pk_fma_f32 v[76:77], v[76:77], s[26:27], v[70:71] op_sel_hi:[1,0,1]
	v_pk_fma_f32 v[108:109], v[132:133], s[26:27], v[108:109] op_sel_hi:[1,0,1]
	v_add_f32_e32 v71, v76, v77
	v_add_f32_e32 v70, v108, v109
	v_add_f32_e32 v70, v70, v71
	v_add_f32_e32 v70, v107, v70
	s_add_i32 s34, s34, s44
	s_mov_b32 s35, 1
	v_add_f32_dpp v70, v70, v70 quad_perm:[1,0,3,2] row_mask:0xf bank_mask:0xf bound_ctrl:1
	s_mov_b64 s[30:31], -1
	s_nop 0
	v_add_f32_dpp v70, v70, v70 quad_perm:[2,3,0,1] row_mask:0xf bank_mask:0xf bound_ctrl:1
	s_nop 1
	v_add_f32_dpp v70, v70, v70 row_half_mirror row_mask:0xf bank_mask:0xf bound_ctrl:1
	s_nop 1
	v_add_f32_dpp v70, v70, v70 row_mirror row_mask:0xf bank_mask:0xf bound_ctrl:1
	v_mov_b32_e32 v71, v70
	s_nop 1
	v_permlane16_swap_b32_e32 v70, v71
	v_add_f32_e32 v70, v70, v71
	v_mov_b32_e32 v71, v70
	s_nop 1
	v_permlane32_swap_b32_e32 v70, v71
	v_add_f32_e32 v70, v70, v71
	v_fmac_f32_e32 v73, 0xba800000, v70
	v_fmac_f32_e32 v75, 0xba800000, v70
	v_fmamk_f32 v72, v70, 0xba800000, v72
	v_fmamk_f32 v74, v70, 0xba800000, v74
	v_mul_f32_e32 v71, v75, v75
	v_mul_f32_e32 v107, v73, v73
	v_fmac_f32_e32 v71, v74, v74
	v_fmac_f32_e32 v107, v72, v72
	v_fmac_f32_e32 v81, 0xba800000, v70
	v_fmac_f32_e32 v111, 0xba800000, v70
	v_add_f32_e32 v71, v71, v107
	v_fmamk_f32 v80, v70, 0xba800000, v80
	v_fmamk_f32 v110, v70, 0xba800000, v110
	v_mul_f32_e32 v107, v111, v111
	v_mul_f32_e32 v114, v81, v81
	v_fmac_f32_e32 v107, v110, v110
	v_fmac_f32_e32 v114, v80, v80
	v_add_f32_e32 v107, v107, v114
	v_fmac_f32_e32 v79, 0xba800000, v70
	v_fmac_f32_e32 v113, 0xba800000, v70
	v_add_f32_e32 v71, v71, v107
	v_fmamk_f32 v78, v70, 0xba800000, v78
	v_fmamk_f32 v112, v70, 0xba800000, v112
	v_mul_f32_e32 v107, v113, v113
	v_mul_f32_e32 v114, v79, v79
	v_fmac_f32_e32 v107, v112, v112
	v_fmac_f32_e32 v114, v78, v78
	v_add_f32_e32 v107, v107, v114
	v_fmac_f32_e32 v77, 0xba800000, v70
	v_fmac_f32_e32 v109, 0xba800000, v70
	v_add_f32_e32 v71, v107, v71
	v_fmamk_f32 v76, v70, 0xba800000, v76
	v_fmamk_f32 v108, v70, 0xba800000, v108
	v_mul_f32_e32 v70, v109, v109
	v_mul_f32_e32 v107, v77, v77
	v_fmac_f32_e32 v70, v108, v108
	v_fmac_f32_e32 v107, v76, v76
	v_add_f32_e32 v70, v70, v107
	v_add_f32_e32 v70, v70, v71
	s_nop 1
	v_add_f32_dpp v70, v70, v70 quad_perm:[1,0,3,2] row_mask:0xf bank_mask:0xf bound_ctrl:1
	s_nop 1
	v_add_f32_dpp v70, v70, v70 quad_perm:[2,3,0,1] row_mask:0xf bank_mask:0xf bound_ctrl:1
	s_nop 1
	v_add_f32_dpp v70, v70, v70 row_half_mirror row_mask:0xf bank_mask:0xf bound_ctrl:1
	s_nop 1
	v_add_f32_dpp v70, v70, v70 row_mirror row_mask:0xf bank_mask:0xf bound_ctrl:1
	v_mov_b32_e32 v71, v70
	s_nop 1
	v_permlane16_swap_b32_e32 v70, v71
	v_add_f32_e32 v70, v70, v71
	v_mov_b32_e32 v71, v70
	s_nop 1
	v_permlane32_swap_b32_e32 v70, v71
	v_add_f32_e32 v70, v70, v71
	v_fmamk_f32 v70, v70, 0x3a800000, v87
	v_mul_f32_e32 v71, 0x4f800000, v70
	v_cmp_gt_f32_e32 vcc, s50, v70
	s_nop 1
	v_cndmask_b32_e32 v70, v70, v71, vcc
	v_sqrt_f32_e32 v71, v70
	s_nop 0
	v_add_u32_e32 v107, -1, v71
	v_fma_f32 v114, -v107, v71, v70
	v_cmp_ge_f32_e64 s[10:11], 0, v114
	v_add_u32_e32 v114, 1, v71
	s_nop 0
	v_cndmask_b32_e64 v107, v71, v107, s[10:11]
	v_fma_f32 v71, -v114, v71, v70
	v_cmp_lt_f32_e64 s[10:11], 0, v71
	s_nop 1
	v_cndmask_b32_e64 v71, v107, v114, s[10:11]
	v_mul_f32_e32 v107, 0x37800000, v71
	v_cndmask_b32_e32 v71, v71, v107, vcc
	v_cmp_class_f32_e32 vcc, v70, v88
	s_nop 1
	v_cndmask_b32_e32 v70, v71, v70, vcc
	v_div_scale_f32 v71, s[10:11], v70, v70, 1.0
	v_rcp_f32_e32 v107, v71
	s_add_i32 s10, s33, s34
	s_ashr_i32 s11, s10, 31
	s_lshl_b64 s[10:11], s[10:11], 12
	v_fma_f32 v114, -v71, v107, 1.0
	v_fmac_f32_e32 v107, v114, v107
	v_div_scale_f32 v114, vcc, 1.0, v70, 1.0
	v_mul_f32_e32 v115, v114, v107
	v_fma_f32 v116, -v71, v115, v114
	v_fmac_f32_e32 v115, v116, v107
	v_fma_f32 v71, -v71, v115, v114
	v_div_fmas_f32 v71, v71, v107, v115
	v_div_fixup_f32 v114, v71, v70, 1.0
	v_pk_mul_f32 v[70:71], v[74:75], v[114:115] op_sel_hi:[1,0]
	v_pk_mul_f32 v[72:73], v[72:73], v[114:115] op_sel_hi:[1,0]
	v_pk_fma_f32 v[70:71], v[16:17], v[70:71], v[24:25]
	v_pk_fma_f32 v[72:73], v[18:19], v[72:73], v[26:27]
	v_lshl_add_u64 v[74:75], v[54:55], 0, s[10:11]
	global_store_dwordx4 v[74:75], v[70:73], off nt
	s_mov_b64 s[10:11], 0
	s_and_b64 vcc, exec, s[28:29]
	v_pk_mul_f32 v[70:71], v[110:111], v[114:115] op_sel_hi:[1,0]
	v_pk_mul_f32 v[72:73], v[80:81], v[114:115] op_sel_hi:[1,0]
	v_pk_fma_f32 v[70:71], v[20:21], v[70:71], v[28:29]
	v_pk_fma_f32 v[72:73], v[22:23], v[72:73], v[30:31]
	global_store_dwordx4 v[74:75], v[70:73], off offset:1024 nt
	s_nop 1
	v_pk_mul_f32 v[70:71], v[112:113], v[114:115] op_sel_hi:[1,0]
	v_pk_mul_f32 v[72:73], v[78:79], v[114:115] op_sel_hi:[1,0]
	v_pk_fma_f32 v[70:71], v[32:33], v[70:71], v[40:41]
	v_pk_fma_f32 v[72:73], v[34:35], v[72:73], v[42:43]
	global_store_dwordx4 v[74:75], v[70:73], off offset:2048 nt
	s_nop 1
	v_pk_mul_f32 v[70:71], v[108:109], v[114:115] op_sel_hi:[1,0]
	v_pk_mul_f32 v[72:73], v[76:77], v[114:115] op_sel_hi:[1,0]
	v_pk_fma_f32 v[70:71], v[36:37], v[70:71], v[44:45]
	v_pk_fma_f32 v[72:73], v[38:39], v[72:73], v[46:47]
	global_store_dwordx4 v[74:75], v[70:73], off offset:3072 nt
	s_cbranch_vccnz .LBB0_3795

.LBB0_3811:
	s_add_i32 s10, s48, s37
	s_add_i32 s11, s35, s36
	s_waitcnt vmcnt(22)
	v_mov_b64_e32 v[64:65], v[78:79]
	s_waitcnt vmcnt(17)
	v_mov_b32_e32 v78, v109
	s_waitcnt vmcnt(16)
	v_mov_b32_e32 v79, v107
	s_add_i32 s38, s10, 1
	s_add_i32 s41, s11, 4
	s_add_i32 s42, s11, 5
	s_add_i32 s51, s11, 6
	v_mov_b64_e32 v[60:61], v[70:71]
	s_waitcnt vmcnt(4)
	v_mov_b32_e32 v70, v108
	v_mov_b32_e32 v71, v112
	v_mov_b32_e32 v72, v115
	v_mov_b32_e32 v73, v117
	v_mov_b32_e32 v91, v116
	v_mov_b32_e32 v123, v114
	v_mov_b32_e32 v126, v113
	s_add_i32 s53, s11, 7
	v_cvt_pk_f32_fp8_e32 v[102:103], v111
	v_cvt_pk_f32_fp8_sdwa v[104:105], v111 src0_sel:WORD_1
	v_cvt_pk_f32_fp8_e32 v[106:107], v110
	v_cvt_pk_f32_fp8_sdwa v[108:109], v110 src0_sel:WORD_1
	v_cvt_pk_f32_fp8_e32 v[110:111], v78
	v_cvt_pk_f32_fp8_sdwa v[112:113], v78 src0_sel:WORD_1
	v_cvt_pk_f32_fp8_e32 v[114:115], v79
	v_cvt_pk_f32_fp8_sdwa v[116:117], v79 src0_sel:WORD_1
	s_ashr_i32 s11, s10, 31
	s_ashr_i32 s39, s38, 31
	v_readlane_b32 s40, v89, s41
	v_readlane_b32 s52, v89, s42
	v_readlane_b32 s54, v89, s51
	v_mov_b64_e32 v[62:63], s[24:25]
	v_readlane_b32 s43, v90, s41
	v_readlane_b32 s42, v90, s42
	v_readlane_b32 s57, v90, s51
	v_readlane_b32 s58, v89, s53
	v_readlane_b32 s56, v90, s53
	s_lshl_b64 s[10:11], s[10:11], 12
	s_lshl_b64 s[38:39], s[38:39], 11
	s_ashr_i32 s41, s40, 31
	s_ashr_i32 s53, s52, 31
	s_ashr_i32 s55, s54, 31
	v_mov_b64_e32 v[66:67], v[80:81]
	v_cvt_pk_f32_fp8_e32 v[136:137], v73
	v_cvt_pk_f32_fp8_sdwa v[138:139], v73 src0_sel:WORD_1
	v_cvt_pk_f32_fp8_e32 v[160:161], v72
	v_cvt_pk_f32_fp8_sdwa v[162:163], v72 src0_sel:WORD_1
	v_cvt_pk_f32_fp8_e32 v[164:165], v71
	v_cvt_pk_f32_fp8_sdwa v[166:167], v71 src0_sel:WORD_1
	v_cvt_pk_f32_fp8_e32 v[168:169], v70
	v_cvt_pk_f32_fp8_sdwa v[170:171], v70 src0_sel:WORD_1
	v_pk_mul_f32 v[70:71], s[42:43], v[62:63] op_sel_hi:[1,0]
	v_pk_mul_f32 v[72:73], s[56:57], v[62:63] op_sel_hi:[1,0]
	s_ashr_i32 s59, s58, 31
	v_lshl_add_u64 v[172:173], v[54:55], 0, s[10:11]
	v_lshl_add_u64 v[62:63], v[50:51], 0, s[38:39]
	s_lshl_b64 s[10:11], s[40:41], 10
	s_lshl_b64 s[38:39], s[52:53], 10
	s_lshl_b64 s[40:41], s[54:55], 10
	v_cvt_f32_f16_sdwa v69, v67 dst_sel:DWORD dst_unused:UNUSED_PAD src0_sel:WORD_1
	v_cvt_f32_f16_sdwa v93, v66 dst_sel:DWORD dst_unused:UNUSED_PAD src0_sel:WORD_1
	v_cvt_f32_f16_e32 v68, v67
	v_cvt_f32_f16_e32 v92, v66
	v_cvt_f32_f16_sdwa v67, v65 dst_sel:DWORD dst_unused:UNUSED_PAD src0_sel:WORD_1
	v_cvt_f32_f16_sdwa v95, v64 dst_sel:DWORD dst_unused:UNUSED_PAD src0_sel:WORD_1
	v_cvt_f32_f16_e32 v66, v65
	v_cvt_f32_f16_e32 v94, v64
	v_cvt_f32_f16_sdwa v65, v77 dst_sel:DWORD dst_unused:UNUSED_PAD src0_sel:WORD_1
	v_cvt_f32_f16_sdwa v97, v76 dst_sel:DWORD dst_unused:UNUSED_PAD src0_sel:WORD_1
	v_cvt_f32_f16_e32 v64, v77
	v_cvt_f32_f16_e32 v96, v76
	v_cvt_f32_f16_sdwa v99, v75 dst_sel:DWORD dst_unused:UNUSED_PAD src0_sel:WORD_1
	v_cvt_f32_f16_sdwa v101, v74 dst_sel:DWORD dst_unused:UNUSED_PAD src0_sel:WORD_1
	v_cvt_f32_f16_e32 v98, v75
	v_cvt_f32_f16_e32 v100, v74
	v_cvt_pk_f32_fp8_e32 v[128:129], v123
	v_cvt_pk_f32_fp8_sdwa v[130:131], v123 src0_sel:WORD_1
	v_cvt_pk_f32_fp8_e32 v[140:141], v118
	v_cvt_pk_f32_fp8_sdwa v[142:143], v118 src0_sel:WORD_1
	v_cvt_pk_f32_fp8_e32 v[144:145], v119
	v_cvt_pk_f32_fp8_sdwa v[146:147], v119 src0_sel:WORD_1
	v_cvt_pk_f32_fp8_e32 v[156:157], v122
	v_cvt_pk_f32_fp8_sdwa v[158:159], v122 src0_sel:WORD_1
	s_lshl_b64 s[42:43], s[58:59], 10
	global_load_dwordx2 v[80:81], v[62:63], off
	global_load_dwordx2 v[78:79], v[62:63], off offset:512
	global_load_dwordx2 v[76:77], v[62:63], off offset:1024
	global_load_dwordx2 v[74:75], v[62:63], off offset:1536
	v_lshl_add_u64 v[62:63], v[52:53], 0, s[10:11]
	v_lshl_add_u64 v[118:119], v[52:53], 0, s[38:39]
	v_lshl_add_u64 v[122:123], v[52:53], 0, s[40:41]
	v_cvt_pk_f32_fp8_e32 v[148:149], v120
	v_cvt_pk_f32_fp8_sdwa v[150:151], v120 src0_sel:WORD_1
	v_cvt_pk_f32_fp8_e32 v[152:153], v121
	v_cvt_pk_f32_fp8_sdwa v[154:155], v121 src0_sel:WORD_1
	v_lshl_add_u64 v[174:175], v[52:53], 0, s[42:43]
	v_pk_fma_f32 v[176:177], v[60:61], v[108:109], 0 op_sel:[1,0,0] op_sel_hi:[1,1,0]
	v_pk_fma_f32 v[178:179], v[60:61], v[106:107], 0 op_sel:[1,0,0] op_sel_hi:[1,1,0]
	v_pk_fma_f32 v[180:181], v[60:61], v[112:113], 0 op_sel:[1,0,0] op_sel_hi:[1,1,0]
	v_pk_fma_f32 v[182:183], v[60:61], v[110:111], 0 op_sel:[1,0,0] op_sel_hi:[1,1,0]
	v_pk_fma_f32 v[184:185], v[60:61], v[116:117], 0 op_sel:[1,0,0] op_sel_hi:[1,1,0]
	v_pk_fma_f32 v[186:187], v[60:61], v[114:115], 0 op_sel:[1,0,0] op_sel_hi:[1,1,0]
	global_load_dword v111, v[62:63], off
	global_load_dword v110, v[62:63], off offset:256
	global_load_dword v109, v[62:63], off offset:512
	global_load_dword v107, v[62:63], off offset:768
	global_load_dword v113, v[118:119], off
	global_load_dword v114, v[118:119], off offset:256
	global_load_dword v116, v[118:119], off offset:512
	global_load_dword v117, v[118:119], off offset:768
	s_nop 0
	global_load_dword v118, v[122:123], off
	global_load_dword v119, v[122:123], off offset:256
	global_load_dword v120, v[122:123], off offset:512
	global_load_dword v121, v[122:123], off offset:768
	s_nop 0
	global_load_dword v122, v[174:175], off
	global_load_dword v115, v[174:175], off offset:256
	global_load_dword v112, v[174:175], off offset:512
	global_load_dword v108, v[174:175], off offset:768
	v_cvt_pk_f32_fp8_e32 v[124:125], v126
	v_cvt_pk_f32_fp8_sdwa v[126:127], v126 src0_sel:WORD_1
	v_cvt_pk_f32_fp8_e32 v[132:133], v91
	v_cvt_pk_f32_fp8_sdwa v[134:135], v91 src0_sel:WORD_1
	v_pk_fma_f32 v[104:105], v[60:61], v[104:105], 0 op_sel:[1,0,0] op_sel_hi:[1,1,0]
	v_pk_fma_f32 v[102:103], v[60:61], v[102:103], 0 op_sel:[1,0,0] op_sel_hi:[1,1,0]
	s_add_i32 s37, s37, 1
	v_pk_fma_f32 v[62:63], v[60:61], v[124:125], v[102:103] op_sel_hi:[0,1,1]
	v_pk_fma_f32 v[102:103], v[60:61], v[126:127], v[104:105] op_sel_hi:[0,1,1]
	v_pk_fma_f32 v[104:105], v[60:61], v[128:129], v[178:179] op_sel_hi:[0,1,1]
	v_pk_fma_f32 v[124:125], v[60:61], v[130:131], v[176:177] op_sel_hi:[0,1,1]
	v_pk_fma_f32 v[126:127], v[60:61], v[132:133], v[182:183] op_sel_hi:[0,1,1]
	v_pk_fma_f32 v[128:129], v[60:61], v[134:135], v[180:181] op_sel_hi:[0,1,1]
	v_pk_fma_f32 v[130:131], v[60:61], v[136:137], v[186:187] op_sel_hi:[0,1,1]
	v_pk_fma_f32 v[60:61], v[60:61], v[138:139], v[184:185] op_sel_hi:[0,1,1]
	v_pk_fma_f32 v[102:103], v[58:59], v[142:143], v[102:103] op_sel:[1,0,0]
	v_pk_fma_f32 v[62:63], v[58:59], v[140:141], v[62:63] op_sel:[1,0,0]
	v_pk_fma_f32 v[124:125], v[58:59], v[146:147], v[124:125] op_sel:[1,0,0]
	v_pk_fma_f32 v[104:105], v[58:59], v[144:145], v[104:105] op_sel:[1,0,0]
	v_pk_fma_f32 v[60:61], v[58:59], v[154:155], v[60:61] op_sel:[1,0,0]
	v_pk_fma_f32 v[62:63], v[58:59], v[156:157], v[62:63] op_sel_hi:[0,1,1]
	v_pk_fma_f32 v[102:103], v[58:59], v[158:159], v[102:103] op_sel_hi:[0,1,1]
	v_pk_fma_f32 v[128:129], v[58:59], v[150:151], v[128:129] op_sel:[1,0,0]
	v_pk_fma_f32 v[126:127], v[58:59], v[148:149], v[126:127] op_sel:[1,0,0]
	v_pk_fma_f32 v[130:131], v[58:59], v[152:153], v[130:131] op_sel:[1,0,0]
	v_pk_fma_f32 v[104:105], v[58:59], v[160:161], v[104:105] op_sel_hi:[0,1,1]
	v_pk_fma_f32 v[124:125], v[58:59], v[162:163], v[124:125] op_sel_hi:[0,1,1]
	v_pk_fma_f32 v[60:61], v[58:59], v[170:171], v[60:61] op_sel_hi:[0,1,1]
	s_waitcnt lgkmcnt(11)
	v_pk_mul_f32 v[102:103], v[102:103], v[2:3]
	v_pk_mul_f32 v[62:63], v[62:63], v[0:1]
	v_pk_fma_f32 v[126:127], v[58:59], v[164:165], v[126:127] op_sel_hi:[0,1,1]
	v_pk_fma_f32 v[128:129], v[58:59], v[166:167], v[128:129] op_sel_hi:[0,1,1]
	v_pk_fma_f32 v[130:131], v[58:59], v[168:169], v[130:131] op_sel_hi:[0,1,1]
	s_waitcnt lgkmcnt(10)
	v_pk_mul_f32 v[124:125], v[6:7], v[124:125]
	v_pk_mul_f32 v[104:105], v[4:5], v[104:105]
	s_waitcnt lgkmcnt(8)
	v_pk_mul_f32 v[60:61], v[14:15], v[60:61]
	v_pk_fma_f32 v[62:63], v[92:93], s[26:27], v[62:63] op_sel_hi:[1,0,1]
	v_pk_fma_f32 v[68:69], v[68:69], s[26:27], v[102:103] op_sel_hi:[1,0,1]
	v_pk_mul_f32 v[128:129], v[10:11], v[128:129]
	v_pk_mul_f32 v[126:127], v[8:9], v[126:127]
	v_pk_mul_f32 v[130:131], v[12:13], v[130:131]
	v_pk_fma_f32 v[92:93], v[94:95], s[26:27], v[104:105] op_sel_hi:[1,0,1]
	v_pk_fma_f32 v[66:67], v[66:67], s[26:27], v[124:125] op_sel_hi:[1,0,1]
	v_pk_fma_f32 v[60:61], v[98:99], s[26:27], v[60:61] op_sel_hi:[1,0,1]
	v_add_f32_e32 v91, v62, v63
	v_add_f32_e32 v98, v68, v69
	v_pk_fma_f32 v[94:95], v[96:97], s[26:27], v[126:127] op_sel_hi:[1,0,1]
	v_pk_fma_f32 v[64:65], v[64:65], s[26:27], v[128:129] op_sel_hi:[1,0,1]
	v_pk_fma_f32 v[96:97], v[100:101], s[26:27], v[130:131] op_sel_hi:[1,0,1]
	v_add_f32_e32 v99, v92, v93
	v_add_f32_e32 v100, v66, v67
	v_add_f32_e32 v91, v91, v98
	v_add_f32_e32 v101, v94, v95
	v_add_f32_e32 v102, v64, v65
	v_add_f32_e32 v98, v99, v100
	v_add_f32_e32 v91, 0, v91
	v_add_f32_e32 v103, v96, v97
	v_add_f32_e32 v104, v60, v61
	v_add_f32_e32 v99, v101, v102
	v_add_f32_e32 v91, v91, v98
	v_add_f32_e32 v100, v103, v104
	v_add_f32_e32 v91, v91, v99
	v_add_f32_e32 v91, v91, v100
	s_add_i32 s36, s36, 4
	s_cmp_eq_u32 s36, 12
	v_add_f32_dpp v91, v91, v91 quad_perm:[1,0,3,2] row_mask:0xf bank_mask:0xf bound_ctrl:1
	v_mov_b64_e32 v[58:59], v[72:73]
	s_nop 0
	v_add_f32_dpp v91, v91, v91 quad_perm:[2,3,0,1] row_mask:0xf bank_mask:0xf bound_ctrl:1
	s_nop 1
	v_add_f32_dpp v91, v91, v91 row_half_mirror row_mask:0xf bank_mask:0xf bound_ctrl:1
	s_nop 1
	v_add_f32_dpp v91, v91, v91 row_mirror row_mask:0xf bank_mask:0xf bound_ctrl:1
	v_mov_b32_e32 v98, v91
	s_nop 1
	v_permlane16_swap_b32_e32 v91, v98
	v_add_f32_e32 v91, v91, v98
	v_mov_b32_e32 v98, v91
	s_nop 1
	v_permlane32_swap_b32_e32 v91, v98
	v_add_f32_e32 v91, v91, v98
	v_fmac_f32_e32 v69, 0xba800000, v91
	v_fmac_f32_e32 v63, 0xba800000, v91
	v_fmac_f32_e32 v67, 0xba800000, v91
	v_fmac_f32_e32 v93, 0xba800000, v91
	v_fmamk_f32 v68, v91, 0xba800000, v68
	v_fmamk_f32 v62, v91, 0xba800000, v62
	v_fmamk_f32 v66, v91, 0xba800000, v66
	v_fmamk_f32 v92, v91, 0xba800000, v92
	v_fmamk_f32 v64, v91, 0xba800000, v64
	v_fmac_f32_e32 v65, 0xba800000, v91
	v_fmamk_f32 v94, v91, 0xba800000, v94
	v_fmac_f32_e32 v95, 0xba800000, v91
	v_fmamk_f32 v60, v91, 0xba800000, v60
	v_fmac_f32_e32 v61, 0xba800000, v91
	v_fmamk_f32 v96, v91, 0xba800000, v96
	v_fmac_f32_e32 v97, 0xba800000, v91
	v_mul_f32_e32 v91, v63, v63
	v_mul_f32_e32 v98, v69, v69
	v_mul_f32_e32 v99, v93, v93
	v_mul_f32_e32 v100, v67, v67
	v_mul_f32_e32 v101, v95, v95
	v_mul_f32_e32 v102, v65, v65
	v_fmac_f32_e32 v91, v62, v62
	v_fmac_f32_e32 v98, v68, v68
	v_fmac_f32_e32 v99, v92, v92
	v_fmac_f32_e32 v100, v66, v66
	v_mul_f32_e32 v103, v97, v97
	v_mul_f32_e32 v104, v61, v61
	v_fmac_f32_e32 v101, v94, v94
	v_fmac_f32_e32 v102, v64, v64
	v_add_f32_e32 v91, v91, v98
	v_add_f32_e32 v98, v99, v100
	v_fmac_f32_e32 v103, v96, v96
	v_fmac_f32_e32 v104, v60, v60
	v_add_f32_e32 v99, v101, v102
	v_add_f32_e32 v91, v91, v98
	v_add_f32_e32 v100, v103, v104
	v_add_f32_e32 v91, v99, v91
	v_add_f32_e32 v91, v100, v91
	s_nop 1
	v_add_f32_dpp v91, v91, v91 quad_perm:[1,0,3,2] row_mask:0xf bank_mask:0xf bound_ctrl:1
	s_nop 1
	v_add_f32_dpp v91, v91, v91 quad_perm:[2,3,0,1] row_mask:0xf bank_mask:0xf bound_ctrl:1
	s_nop 1
	v_add_f32_dpp v91, v91, v91 row_half_mirror row_mask:0xf bank_mask:0xf bound_ctrl:1
	s_nop 1
	v_add_f32_dpp v91, v91, v91 row_mirror row_mask:0xf bank_mask:0xf bound_ctrl:1
	v_mov_b32_e32 v98, v91
	s_nop 1
	v_permlane16_swap_b32_e32 v91, v98
	v_add_f32_e32 v91, v91, v98
	v_mov_b32_e32 v98, v91
	s_nop 1
	v_permlane32_swap_b32_e32 v91, v98
	v_add_f32_e32 v91, v91, v98
	v_fmamk_f32 v91, v91, 0x3a800000, v87
	v_mul_f32_e32 v98, 0x4f800000, v91
	v_cmp_gt_f32_e32 vcc, s50, v91
	s_nop 1
	v_cndmask_b32_e32 v91, v91, v98, vcc
	v_sqrt_f32_e32 v98, v91
	s_nop 0
	v_add_u32_e32 v99, -1, v98
	v_add_u32_e32 v100, 1, v98
	v_fma_f32 v101, -v99, v98, v91
	v_fma_f32 v102, -v100, v98, v91
	v_cmp_ge_f32_e64 s[10:11], 0, v101
	s_nop 1
	v_cndmask_b32_e64 v98, v98, v99, s[10:11]
	v_cmp_lt_f32_e64 s[10:11], 0, v102
	s_nop 1
	v_cndmask_b32_e64 v98, v98, v100, s[10:11]
	v_mul_f32_e32 v99, 0x37800000, v98
	v_cndmask_b32_e32 v98, v98, v99, vcc
	v_cmp_class_f32_e32 vcc, v91, v88
	s_nop 1
	v_cndmask_b32_e32 v91, v98, v91, vcc
	v_div_scale_f32 v98, s[10:11], v91, v91, 1.0
	v_rcp_f32_e32 v100, v98
	v_div_scale_f32 v99, vcc, 1.0, v91, 1.0
	v_fma_f32 v101, -v98, v100, 1.0
	v_fmac_f32_e32 v100, v101, v100
	v_mul_f32_e32 v101, v99, v100
	v_fma_f32 v102, -v98, v101, v99
	v_fmac_f32_e32 v101, v102, v100
	v_fma_f32 v98, -v98, v101, v99
	v_div_fmas_f32 v98, v98, v100, v101
	v_div_fixup_f32 v98, v98, v91, 1.0
	v_pk_mul_f32 v[100:101], v[62:63], v[98:99] op_sel_hi:[1,0]
	v_pk_mul_f32 v[62:63], v[68:69], v[98:99] op_sel_hi:[1,0]
	v_pk_mul_f32 v[68:69], v[92:93], v[98:99] op_sel_hi:[1,0]
	v_pk_mul_f32 v[66:67], v[66:67], v[98:99] op_sel_hi:[1,0]
	v_pk_mul_f32 v[92:93], v[94:95], v[98:99] op_sel_hi:[1,0]
	v_pk_mul_f32 v[94:95], v[64:65], v[98:99] op_sel_hi:[1,0]
	v_pk_mul_f32 v[96:97], v[96:97], v[98:99] op_sel_hi:[1,0]
	v_pk_mul_f32 v[98:99], v[60:61], v[98:99] op_sel_hi:[1,0]
	s_waitcnt lgkmcnt(5)
	v_pk_fma_f32 v[62:63], v[18:19], v[62:63], v[26:27]
	v_pk_fma_f32 v[60:61], v[16:17], v[100:101], v[24:25]
	s_waitcnt lgkmcnt(4)
	v_pk_fma_f32 v[66:67], v[22:23], v[66:67], v[30:31]
	v_pk_fma_f32 v[64:65], v[20:21], v[68:69], v[28:29]
	s_waitcnt lgkmcnt(1)
	v_pk_fma_f32 v[94:95], v[34:35], v[94:95], v[42:43]
	v_pk_fma_f32 v[92:93], v[32:33], v[92:93], v[40:41]
	s_waitcnt lgkmcnt(0)
	v_pk_fma_f32 v[98:99], v[38:39], v[98:99], v[46:47]
	v_pk_fma_f32 v[96:97], v[36:37], v[96:97], v[44:45]
	global_store_dwordx4 v[172:173], v[60:63], off nt
	global_store_dwordx4 v[172:173], v[64:67], off offset:1024 nt
	global_store_dwordx4 v[172:173], v[92:95], off offset:2048 nt
	global_store_dwordx4 v[172:173], v[96:99], off offset:3072 nt
	s_cbranch_scc0 .LBB0_3811
	s_andn2_b64 vcc, exec, s[30:31]
	s_waitcnt vmcnt(4)
	v_mov_b32_e32 v106, v108
	v_mov_b32_e32 v105, v112
	v_mov_b32_e32 v104, v115
	v_mov_b32_e32 v103, v122
	v_mov_b32_e32 v102, v121
	v_mov_b32_e32 v101, v120
	v_mov_b32_e32 v100, v119
	v_mov_b32_e32 v99, v118
	v_mov_b32_e32 v94, v117
	v_mov_b32_e32 v93, v116
	v_mov_b32_e32 v92, v114
	v_mov_b32_e32 v91, v113
	v_mov_b32_e32 v98, v107
	v_mov_b32_e32 v97, v109
	v_mov_b32_e32 v96, v110
	v_mov_b32_e32 v95, v111
	v_mov_b64_e32 v[66:67], v[74:75]
	v_mov_b64_e32 v[64:65], v[76:77]
	v_mov_b64_e32 v[62:63], v[78:79]
	v_mov_b64_e32 v[60:61], v[80:81]
	v_mov_b64_e32 v[58:59], v[72:73]
	v_mov_b64_e32 v[68:69], v[70:71]
	s_cbranch_vccnz .LBB0_3809
	v_readlane_b32 s10, v89, 16
	s_ashr_i32 s11, s10, 31
	s_lshl_b64 s[10:11], s[10:11], 10
	v_lshl_add_u64 v[58:59], v[52:53], 0, s[10:11]
	v_readlane_b32 s10, v89, 17
	s_ashr_i32 s11, s10, 31
	s_lshl_b64 s[10:11], s[10:11], 10
	v_lshl_add_u64 v[68:69], v[52:53], 0, s[10:11]
	v_readlane_b32 s10, v89, 18
	s_ashr_i32 s11, s10, 31
	s_lshl_b64 s[10:11], s[10:11], 10
	global_load_dwordx2 v[60:61], v[56:57], off
	global_load_dwordx2 v[62:63], v[56:57], off offset:512
	global_load_dwordx2 v[64:65], v[56:57], off offset:1024
	global_load_dwordx2 v[66:67], v[56:57], off offset:1536
	global_load_dword v95, v[58:59], off
	global_load_dword v96, v[58:59], off offset:256
	global_load_dword v97, v[58:59], off offset:512
	global_load_dword v98, v[58:59], off offset:768
	global_load_dword v91, v[68:69], off
	global_load_dword v92, v[68:69], off offset:256
	global_load_dword v93, v[68:69], off offset:512
	global_load_dword v94, v[68:69], off offset:768
	v_lshl_add_u64 v[58:59], v[52:53], 0, s[10:11]
	v_readlane_b32 s10, v89, 19
	s_ashr_i32 s11, s10, 31
	s_lshl_b64 s[10:11], s[10:11], 10
	v_lshl_add_u64 v[68:69], v[52:53], 0, s[10:11]
	global_load_dword v99, v[58:59], off
	global_load_dword v100, v[58:59], off offset:256
	global_load_dword v101, v[58:59], off offset:512
	global_load_dword v102, v[58:59], off offset:768
	global_load_dword v103, v[68:69], off
	global_load_dword v104, v[68:69], off offset:256
	global_load_dword v105, v[68:69], off offset:512
	global_load_dword v106, v[68:69], off offset:768
	v_readlane_b32 s11, v90, 16
	v_readlane_b32 s10, v90, 17
	v_mov_b64_e32 v[58:59], s[24:25]
	s_nop 0
	v_pk_mul_f32 v[68:69], s[10:11], v[58:59] op_sel_hi:[1,0]
	v_readlane_b32 s11, v90, 18
	v_readlane_b32 s10, v90, 19
	s_nop 1
	v_pk_mul_f32 v[58:59], s[10:11], v[58:59] op_sel_hi:[1,0]
	s_branch .LBB0_3809
